# accumulator initialisation with 64-bit moves: attention score-accumulator init (v_mov_b64) and the GEMM per-unit accumulator zeroing (63 fewer VALU ops per unit)
# speedup vs baseline: 1.0100x; 1.0100x over previous
; template <class Epi, class Sched, bool GATHER, bool FP8 = false>
; __device__ __forceinline__ void gemm_phase(LAS unsigned char* lds, const Gemm g, const Sched& S, const Epi& E, const int wave_s) {
;     ...
;         const bool has_next = S.next(ui + 1, nxt);
;         const char* nB = has_next ? (const char*)g.Bt + (size_t)nxt.pn * tstepB : cB;
;         const char* nA = (GATHER || !has_next) ? cA : (const char*)g.A + (size_t)nxt.pm * tstepA;
;     ...
; #pragma unroll
;         for (int a = 0; a < 2; ++a)
; #pragma unroll
;             for (int b = 0; b < 2; ++b)
; #pragma unroll
;                 for (int m = 0; m < 4; ++m)
; #pragma unroll
;                     for (int n = 0; n < 2; ++n) acc[a][b][m][n] = (f32x4){0.f, 0.f, 0.f, 0.f};
;         cur = nxt; cB = nB; cA = nA; ++ui;
.LBB0_203:
	s_ashr_i32 s13, s12, 31
	s_lshl_b64 s[16:17], s[12:13], 18
	s_add_u32 s16, s31, s16
	s_addc_u32 s17, s48, s17
	s_and_b64 s[18:19], s[40:41], exec
	s_cselect_b32 s13, s17, s45
	s_cselect_b32 s58, s16, s44
	s_ashr_i32 s15, s14, 31
	s_lshl_b64 s[18:19], s[14:15], 18
	v_readlane_b32 s2, v246, 23
	v_readlane_b32 s3, v246, 24
	s_add_u32 s18, s2, s18
	s_addc_u32 s19, s3, s19
	s_and_b64 s[42:43], s[40:41], exec
	s_cselect_b32 s15, s19, s1
	s_cselect_b32 s59, s18, s0
	s_add_u32 s42, s0, 0x80
	s_addc_u32 s43, s1, 0
	s_add_u32 s0, s44, 0x100
	v_mov_b32_e32 v40, 0
	s_addc_u32 s1, s45, 0
	s_mov_b32 s60, -2
	v_mov_b32_e32 v41, v40
	v_mov_b64_e32 v[42:43], 0
	v_mov_b64_e32 v[48:49], 0
	v_mov_b64_e32 v[50:51], 0
	v_mov_b64_e32 v[64:65], 0
	v_mov_b64_e32 v[66:67], 0
	v_mov_b64_e32 v[72:73], 0
	v_mov_b64_e32 v[74:75], 0
	v_mov_b64_e32 v[32:33], 0
	v_mov_b64_e32 v[34:35], 0
	v_mov_b64_e32 v[36:37], 0
	v_mov_b64_e32 v[38:39], 0
	v_mov_b64_e32 v[44:45], 0
	v_mov_b64_e32 v[46:47], 0
	v_mov_b64_e32 v[52:53], 0
	v_mov_b64_e32 v[54:55], 0
	v_mov_b64_e32 v[68:69], 0
	v_mov_b64_e32 v[70:71], 0
	v_mov_b64_e32 v[76:77], 0
	v_mov_b64_e32 v[78:79], 0
	v_mov_b64_e32 v[88:89], 0
	v_mov_b64_e32 v[90:91], 0
	v_mov_b64_e32 v[92:93], 0
	v_mov_b64_e32 v[94:95], 0
	v_mov_b64_e32 v[96:97], 0
	v_mov_b64_e32 v[98:99], 0
	v_mov_b64_e32 v[100:101], 0
	v_mov_b64_e32 v[102:103], 0
	v_mov_b64_e32 v[104:105], 0
	v_mov_b64_e32 v[106:107], 0
	v_mov_b64_e32 v[112:113], 0
	v_mov_b64_e32 v[114:115], 0
	v_mov_b64_e32 v[120:121], 0
	v_mov_b64_e32 v[122:123], 0
	v_mov_b64_e32 v[128:129], 0
	v_mov_b64_e32 v[130:131], 0
	v_mov_b64_e32 v[136:137], 0
	v_mov_b64_e32 v[138:139], 0
	v_mov_b64_e32 v[144:145], 0
	v_mov_b64_e32 v[146:147], 0
	v_mov_b64_e32 v[108:109], 0
	v_mov_b64_e32 v[110:111], 0
	v_mov_b64_e32 v[116:117], 0
	v_mov_b64_e32 v[118:119], 0
	v_mov_b64_e32 v[124:125], 0
	v_mov_b64_e32 v[126:127], 0
	v_mov_b64_e32 v[132:133], 0
	v_mov_b64_e32 v[134:135], 0
	v_mov_b64_e32 v[140:141], 0
	v_mov_b64_e32 v[142:143], 0
	v_mov_b64_e32 v[148:149], 0
	v_mov_b64_e32 v[150:151], 0
	v_mov_b64_e32 v[154:155], 0
	v_mov_b64_e32 v[156:157], 0
	v_mov_b64_e32 v[158:159], 0
	v_mov_b64_e32 v[160:161], 0
	v_mov_b64_e32 v[84:85], 0
	v_mov_b64_e32 v[86:87], 0
	v_mov_b64_e32 v[80:81], 0
	v_mov_b64_e32 v[82:83], 0
	v_mov_b64_e32 v[60:61], 0
	v_mov_b64_e32 v[62:63], 0
	v_mov_b64_e32 v[56:57], 0
	v_mov_b64_e32 v[58:59], 0

; template <class Epi, class Sched, bool GATHER, bool FP8 = false>
; __device__ __forceinline__ void gemm_phase(LAS unsigned char* lds, const Gemm g, const Sched& S, const Epi& E, const int wave_s) {
;     ...
;         const bool has_next = S.next(ui + 1, nxt);
;         const char* nB = has_next ? (const char*)g.Bt + (size_t)nxt.pn * tstepB : cB;
;         const char* nA = (GATHER || !has_next) ? cA : (const char*)g.A + (size_t)nxt.pm * tstepA;
;     ...
; #pragma unroll
;         for (int a = 0; a < 2; ++a)
; #pragma unroll
;             for (int b = 0; b < 2; ++b)
; #pragma unroll
;                 for (int m = 0; m < 4; ++m)
; #pragma unroll
;                     for (int n = 0; n < 2; ++n) acc[a][b][m][n] = (f32x4){0.f, 0.f, 0.f, 0.f};
;         cur = nxt; cB = nB; cA = nA; ++ui;
.LBB0_436:
	s_add_u32 s16, s0, 0x80
	s_addc_u32 s17, s1, 0
	s_add_u32 s44, s18, 0x100
	v_mov_b32_e32 v8, 0
	s_addc_u32 s45, s19, 0
	s_mov_b32 s59, -2
	v_mov_b32_e32 v9, v8
	v_mov_b64_e32 v[10:11], 0
	v_mov_b64_e32 v[16:17], 0
	v_mov_b64_e32 v[18:19], 0
	v_mov_b64_e32 v[24:25], 0
	v_mov_b64_e32 v[26:27], 0
	v_mov_b64_e32 v[40:41], 0
	v_mov_b64_e32 v[42:43], 0
	v_mov_b64_e32 v[0:1], 0
	v_mov_b64_e32 v[2:3], 0
	v_mov_b64_e32 v[4:5], 0
	v_mov_b64_e32 v[6:7], 0
	v_mov_b64_e32 v[12:13], 0
	v_mov_b64_e32 v[14:15], 0
	v_mov_b64_e32 v[20:21], 0
	v_mov_b64_e32 v[22:23], 0
	v_mov_b64_e32 v[28:29], 0
	v_mov_b64_e32 v[30:31], 0
	v_mov_b64_e32 v[44:45], 0
	v_mov_b64_e32 v[46:47], 0
	v_mov_b64_e32 v[56:57], 0
	v_mov_b64_e32 v[58:59], 0
	v_mov_b64_e32 v[60:61], 0
	v_mov_b64_e32 v[62:63], 0
	v_mov_b64_e32 v[64:65], 0
	v_mov_b64_e32 v[66:67], 0
	v_mov_b64_e32 v[68:69], 0
	v_mov_b64_e32 v[70:71], 0
	v_mov_b64_e32 v[72:73], 0
	v_mov_b64_e32 v[74:75], 0
	v_mov_b64_e32 v[80:81], 0
	v_mov_b64_e32 v[82:83], 0
	v_mov_b64_e32 v[88:89], 0
	v_mov_b64_e32 v[90:91], 0
	v_mov_b64_e32 v[96:97], 0
	v_mov_b64_e32 v[98:99], 0
	v_mov_b64_e32 v[104:105], 0
	v_mov_b64_e32 v[106:107], 0
	v_mov_b64_e32 v[112:113], 0
	v_mov_b64_e32 v[114:115], 0
	v_mov_b64_e32 v[76:77], 0
	v_mov_b64_e32 v[78:79], 0
	v_mov_b64_e32 v[84:85], 0
	v_mov_b64_e32 v[86:87], 0
	v_mov_b64_e32 v[92:93], 0
	v_mov_b64_e32 v[94:95], 0
	v_mov_b64_e32 v[100:101], 0
	v_mov_b64_e32 v[102:103], 0
	v_mov_b64_e32 v[108:109], 0
	v_mov_b64_e32 v[110:111], 0
	v_mov_b64_e32 v[116:117], 0
	v_mov_b64_e32 v[118:119], 0
	v_mov_b64_e32 v[120:121], 0
	v_mov_b64_e32 v[122:123], 0
	v_mov_b64_e32 v[124:125], 0
	v_mov_b64_e32 v[126:127], 0
	v_mov_b64_e32 v[52:53], 0
	v_mov_b64_e32 v[54:55], 0
	v_mov_b64_e32 v[48:49], 0
	v_mov_b64_e32 v[50:51], 0
	v_mov_b64_e32 v[36:37], 0
	v_mov_b64_e32 v[38:39], 0
	v_mov_b64_e32 v[32:33], 0
	v_mov_b64_e32 v[34:35], 0

; template <class Epi, class Sched, bool GATHER, bool FP8 = false>
; __device__ __forceinline__ void gemm_phase(LAS unsigned char* lds, const Gemm g, const Sched& S, const Epi& E, const int wave_s) {
;     ...
;         const bool has_next = S.next(ui + 1, nxt);
;         const char* nB = has_next ? (const char*)g.Bt + (size_t)nxt.pn * tstepB : cB;
;         const char* nA = (GATHER || !has_next) ? cA : (const char*)g.A + (size_t)nxt.pm * tstepA;
;     ...
; #pragma unroll
;         for (int a = 0; a < 2; ++a)
; #pragma unroll
;             for (int b = 0; b < 2; ++b)
; #pragma unroll
;                 for (int m = 0; m < 4; ++m)
; #pragma unroll
;                     for (int n = 0; n < 2; ++n) acc[a][b][m][n] = (f32x4){0.f, 0.f, 0.f, 0.f};
;         cur = nxt; cB = nB; cA = nA; ++ui;
.LBB0_452:
	s_ashr_i32 s13, s12, 31
	s_lshl_b64 s[0:1], s[12:13], 17
	s_add_u32 s16, s60, s0
	s_addc_u32 s17, s61, s1
	s_and_b64 s[0:1], s[42:43], exec
	s_cselect_b32 s0, s17, s45
	s_cselect_b32 s1, s16, s44
	s_ashr_i32 s15, s14, 31
	s_lshl_b64 s[18:19], s[14:15], 17
	s_add_u32 s18, s92, s18
	s_addc_u32 s19, s93, s19
	s_and_b64 s[40:41], s[42:43], exec
	v_mov_b32_e32 v8, 0
	s_cselect_b32 s13, s19, s47
	s_cselect_b32 s15, s18, s46
	s_mov_b64 s[52:53], 0
	s_mov_b64 s[48:49], -1
	s_mov_b64 s[50:51], 0
	v_mov_b32_e32 v9, v8
	v_mov_b64_e32 v[10:11], 0
	v_mov_b64_e32 v[20:21], 0
	v_mov_b64_e32 v[22:23], 0
	v_mov_b64_e32 v[36:37], 0
	v_mov_b64_e32 v[38:39], 0
	v_mov_b64_e32 v[44:45], 0
	v_mov_b64_e32 v[46:47], 0
	v_mov_b64_e32 v[0:1], 0
	v_mov_b64_e32 v[2:3], 0
	v_mov_b64_e32 v[4:5], 0
	v_mov_b64_e32 v[6:7], 0
	v_mov_b64_e32 v[12:13], 0
	v_mov_b64_e32 v[14:15], 0
	v_mov_b64_e32 v[16:17], 0
	v_mov_b64_e32 v[18:19], 0
	v_mov_b64_e32 v[32:33], 0
	v_mov_b64_e32 v[34:35], 0
	v_mov_b64_e32 v[40:41], 0
	v_mov_b64_e32 v[42:43], 0
	v_mov_b64_e32 v[56:57], 0
	v_mov_b64_e32 v[58:59], 0
	v_mov_b64_e32 v[60:61], 0
	v_mov_b64_e32 v[62:63], 0
	v_mov_b64_e32 v[64:65], 0
	v_mov_b64_e32 v[66:67], 0
	v_mov_b64_e32 v[68:69], 0
	v_mov_b64_e32 v[70:71], 0
	v_mov_b64_e32 v[76:77], 0
	v_mov_b64_e32 v[78:79], 0
	v_mov_b64_e32 v[84:85], 0
	v_mov_b64_e32 v[86:87], 0
	v_mov_b64_e32 v[92:93], 0
	v_mov_b64_e32 v[94:95], 0
	v_mov_b64_e32 v[100:101], 0
	v_mov_b64_e32 v[102:103], 0
	v_mov_b64_e32 v[108:109], 0
	v_mov_b64_e32 v[110:111], 0
	v_mov_b64_e32 v[116:117], 0
	v_mov_b64_e32 v[118:119], 0
	v_mov_b64_e32 v[72:73], 0
	v_mov_b64_e32 v[74:75], 0
	v_mov_b64_e32 v[80:81], 0
	v_mov_b64_e32 v[82:83], 0
	v_mov_b64_e32 v[88:89], 0
	v_mov_b64_e32 v[90:91], 0
	v_mov_b64_e32 v[96:97], 0
	v_mov_b64_e32 v[98:99], 0
	v_mov_b64_e32 v[104:105], 0
	v_mov_b64_e32 v[106:107], 0
	v_mov_b64_e32 v[112:113], 0
	v_mov_b64_e32 v[114:115], 0
	v_mov_b64_e32 v[120:121], 0
	v_mov_b64_e32 v[122:123], 0
	v_mov_b64_e32 v[124:125], 0
	v_mov_b64_e32 v[126:127], 0
	v_mov_b64_e32 v[48:49], 0
	v_mov_b64_e32 v[50:51], 0
	v_mov_b64_e32 v[52:53], 0
	v_mov_b64_e32 v[54:55], 0
	v_mov_b64_e32 v[24:25], 0
	v_mov_b64_e32 v[26:27], 0
	v_mov_b64_e32 v[28:29], 0
	v_mov_b64_e32 v[30:31], 0

; template <class Epi, class Sched, bool GATHER, bool FP8 = false>
; __device__ __forceinline__ void gemm_phase(LAS unsigned char* lds, const Gemm g, const Sched& S, const Epi& E, const int wave_s) {
;     ...
;         const bool has_next = S.next(ui + 1, nxt);
;         const char* nB = has_next ? (const char*)g.Bt + (size_t)nxt.pn * tstepB : cB;
;         const char* nA = (GATHER || !has_next) ? cA : (const char*)g.A + (size_t)nxt.pm * tstepA;
;     ...
; #pragma unroll
;         for (int a = 0; a < 2; ++a)
; #pragma unroll
;             for (int b = 0; b < 2; ++b)
; #pragma unroll
;                 for (int m = 0; m < 4; ++m)
; #pragma unroll
;                     for (int n = 0; n < 2; ++n) acc[a][b][m][n] = (f32x4){0.f, 0.f, 0.f, 0.f};
;         cur = nxt; cB = nB; cA = nA; ++ui;
.LBB0_468:
	s_ashr_i32 s13, s12, 31
	s_lshl_b64 s[0:1], s[12:13], 17
	s_add_u32 s16, s92, s0
	s_addc_u32 s17, s93, s1
	s_and_b64 s[0:1], s[42:43], exec
	s_cselect_b32 s0, s17, s47
	s_cselect_b32 s1, s16, s46
	s_ashr_i32 s15, s14, 31
	s_lshl_b64 s[18:19], s[14:15], 17
	s_add_u32 s18, s60, s18
	s_addc_u32 s19, s61, s19
	s_and_b64 s[40:41], s[42:43], exec
	v_mov_b32_e32 v0, 0
	s_cselect_b32 s13, s19, s45
	s_cselect_b32 s15, s18, s44
	s_mov_b64 s[52:53], 0
	s_mov_b64 s[48:49], -1
	s_mov_b64 s[50:51], 0
	v_mov_b32_e32 v1, v0
	v_mov_b64_e32 v[2:3], 0
	v_mov_b64_e32 v[4:5], 0
	v_mov_b64_e32 v[6:7], 0
	v_mov_b64_e32 v[8:9], 0
	v_mov_b64_e32 v[10:11], 0
	v_mov_b64_e32 v[12:13], 0
	v_mov_b64_e32 v[14:15], 0
	v_mov_b64_e32 v[56:57], 0
	v_mov_b64_e32 v[58:59], 0
	v_mov_b64_e32 v[60:61], 0
	v_mov_b64_e32 v[62:63], 0
	v_mov_b64_e32 v[72:73], 0
	v_mov_b64_e32 v[74:75], 0
	v_mov_b64_e32 v[76:77], 0
	v_mov_b64_e32 v[78:79], 0
	v_mov_b64_e32 v[80:81], 0
	v_mov_b64_e32 v[82:83], 0
	v_mov_b64_e32 v[84:85], 0
	v_mov_b64_e32 v[86:87], 0
	v_mov_b64_e32 v[88:89], 0
	v_mov_b64_e32 v[90:91], 0
	v_mov_b64_e32 v[92:93], 0
	v_mov_b64_e32 v[94:95], 0
	v_mov_b64_e32 v[32:33], 0
	v_mov_b64_e32 v[34:35], 0
	v_mov_b64_e32 v[36:37], 0
	v_mov_b64_e32 v[38:39], 0
	v_mov_b64_e32 v[40:41], 0
	v_mov_b64_e32 v[42:43], 0
	v_mov_b64_e32 v[44:45], 0
	v_mov_b64_e32 v[46:47], 0
	v_mov_b64_e32 v[48:49], 0
	v_mov_b64_e32 v[50:51], 0
	v_mov_b64_e32 v[52:53], 0
	v_mov_b64_e32 v[54:55], 0
	v_mov_b64_e32 v[64:65], 0
	v_mov_b64_e32 v[66:67], 0
	v_mov_b64_e32 v[68:69], 0
	v_mov_b64_e32 v[70:71], 0
	v_mov_b64_e32 v[96:97], 0
	v_mov_b64_e32 v[98:99], 0
	v_mov_b64_e32 v[100:101], 0
	v_mov_b64_e32 v[102:103], 0
	v_mov_b64_e32 v[104:105], 0
	v_mov_b64_e32 v[106:107], 0
	v_mov_b64_e32 v[108:109], 0
	v_mov_b64_e32 v[110:111], 0
	v_mov_b64_e32 v[112:113], 0
	v_mov_b64_e32 v[114:115], 0
	v_mov_b64_e32 v[116:117], 0
	v_mov_b64_e32 v[118:119], 0
	v_mov_b64_e32 v[120:121], 0
	v_mov_b64_e32 v[122:123], 0
	v_mov_b64_e32 v[124:125], 0
	v_mov_b64_e32 v[126:127], 0
	v_mov_b64_e32 v[24:25], 0
	v_mov_b64_e32 v[26:27], 0
	v_mov_b64_e32 v[28:29], 0
	v_mov_b64_e32 v[30:31], 0
	v_mov_b64_e32 v[16:17], 0
	v_mov_b64_e32 v[18:19], 0
	v_mov_b64_e32 v[20:21], 0
	v_mov_b64_e32 v[22:23], 0

; __device__ __forceinline__ void partialSM(f32x16& p0, f32x16& p1, float& m_reg, float& alpha, const bool first) {
;     float ma = max3f(p0[0], p0[1], p0[2]), mb = max3f(p0[3], p0[4], p0[5]), mc = max3f(p0[6], p0[7], p0[8]), md = max3f(p0[9], p0[10], p0[11]);
;     ma = max3f(ma, p0[12], p0[13]); mb = max3f(mb, p0[14], p0[15]); mc = max3f(mc, p1[0], p1[1]); md = max3f(md, p1[2], p1[3]);
;     ma = max3f(ma, p1[4], p1[5]); mb = max3f(mb, p1[6], p1[7]); mc = max3f(mc, p1[8], p1[9]); md = max3f(md, p1[10], p1[11]);
;     ma = max3f(ma, p1[12], p1[13]); mb = max3f(mb, p1[14], p1[15]);
;     float pmax = fmaxf(max3f(ma, mb, mc), md);
;     { auto rr = __builtin_amdgcn_permlane32_swap(__float_as_uint(pmax), __float_as_uint(pmax), false, false);
;       pmax = fmaxf(__uint_as_float(rr[0]), __uint_as_float(rr[1])); }
;     const float u = pmax - PSH;
;     if (__builtin_expect(!first && __all(u <= THR2), 1)) { alpha = 1.f; }
;     else { const float dl = first ? u : fmaxf(u, 0.f); alpha = __builtin_amdgcn_exp2f(-dl); m_reg += dl;
; #pragma unroll
;         for (int r = 0; r < 16; ++r) { p0[r] -= dl; p1[r] -= dl; } }
; #pragma unroll
;     for (int r = 0; r < 16; ++r) p0[r] = __builtin_amdgcn_exp2f(p0[r]);
; }
; __device__ __forceinline__ void finishSM(f32x16& p0, f32x16& p1, float alpha, float& l_reg, v8i& pa) {
; #pragma unroll
;     for (int r = 0; r < 16; ++r) p1[r] = __builtin_amdgcn_exp2f(p1[r]);
;     float sa = p0[0] + p0[1], sb = p0[2] + p0[3], sc = p0[4] + p0[5], sd = p0[6] + p0[7];
;     sa += p0[8]; sb += p0[9]; sc += p0[10]; sd += p0[11]; sa += p0[12]; sb += p0[13]; sc += p0[14]; sd += p0[15];
; #pragma unroll
;     for (int r = 0; r < 16; r += 4) { sa += p1[r]; sb += p1[r + 1]; sc += p1[r + 2]; sd += p1[r + 3]; }
;     float ps = (sa + sb) + (sc + sd);
;     { auto rr = __builtin_amdgcn_permlane32_swap(__float_as_uint(ps), __float_as_uint(ps), false, false);
;       ps = __uint_as_float(rr[0]) + __uint_as_float(rr[1]); }
;     l_reg = l_reg * alpha + ps;
; #pragma unroll
;     for (int c = 0; c < 4; ++c) { pa[c] = (int)pk4_fp8(p0[4 * c], p0[4 * c + 1], p0[4 * c + 2], p0[4 * c + 3]);
;         pa[4 + c] = (int)pk4_fp8(p1[4 * c], p1[4 * c + 1], p1[4 * c + 2], p1[4 * c + 3]); }
; }
; __device__ __forceinline__ void qkt(f32x16& p0, f32x16& p1, const float m_reg, const char* Ks, const v8i* q8, int r32, int hi) {
;     { const float ini = PSH - m_reg;
.LBB0_553:
	v_sub_f32_e32 v80, 0x40400000, v180
	v_mov_b32_e32 v81, v80
	v_mov_b64_e32 v[82:83], v[80:81]
	v_mov_b64_e32 v[84:85], v[80:81]
	v_mov_b64_e32 v[86:87], v[80:81]
	v_mov_b64_e32 v[88:89], v[80:81]
	v_mov_b64_e32 v[90:91], v[80:81]
	v_mov_b64_e32 v[92:93], v[80:81]
	v_mov_b64_e32 v[94:95], v[80:81]
	v_exp_f32_e32 v228, v64
	v_exp_f32_e32 v230, v65
	s_waitcnt lgkmcnt(0)
	v_mfma_scale_f32_32x32x64_f8f6f4 v[96:111], v[96:103], v[120:127], v[80:95], v201, v200 op_sel_hi:[0,0,0]
	v_exp_f32_e32 v222, v66
	v_exp_f32_e32 v223, v67
	v_exp_f32_e32 v229, v68
	v_exp_f32_e32 v231, v69
	v_exp_f32_e32 v226, v70
	v_exp_f32_e32 v227, v71
	v_add_f32_e32 v64, v215, v216
	v_add_f32_e32 v65, v190, v192
	v_add_f32_e32 v66, v213, v214
	v_add_f32_e32 v67, v195, v212
	v_exp_f32_e32 v224, v72
	v_exp_f32_e32 v225, v73
	v_exp_f32_e32 v184, v74
	v_exp_f32_e32 v217, v75
	v_add_f32_e32 v64, v194, v64
	v_mfma_scale_f32_32x32x64_f8f6f4 v[80:95], v[136:143], v[120:127], v[80:95], v201, v200 op_sel_hi:[0,0,0]
	ds_read_b128 v[136:139], v164 offset:64
	ds_read_b128 v[140:143], v164 offset:80
	ds_read_b128 v[144:147], v164 offset:6720
	ds_read_b128 v[148:151], v164 offset:6736
	v_add_f32_e32 v65, v211, v65
	v_add_f32_e32 v66, v186, v66
	v_add_f32_e32 v67, v187, v67
	v_exp_f32_e32 v220, v76
	v_exp_f32_e32 v221, v77
	v_exp_f32_e32 v218, v78
	v_exp_f32_e32 v219, v79
	v_add_f32_e32 v64, v191, v64
	v_add_f32_e32 v65, v193, v65
	v_add_f32_e32 v66, v188, v66
	v_add_f32_e32 v67, v189, v67
	v_add_f32_e32 v64, v228, v64
	v_add_f32_e32 v65, v230, v65
	v_add_f32_e32 v66, v222, v66
	s_waitcnt lgkmcnt(0)
	v_mfma_scale_f32_32x32x64_f8f6f4 v[96:111], v[136:143], v[128:135], v[96:111], v201, v200 op_sel_hi:[0,0,0]
	v_add_f32_e32 v67, v223, v67
	v_add_f32_e32 v64, v229, v64
	v_add_f32_e32 v65, v231, v65
	v_add_f32_e32 v66, v226, v66
	v_add_f32_e32 v67, v227, v67
	v_add_f32_e32 v64, v224, v64
	v_add_f32_e32 v65, v225, v65
	v_add_f32_e32 v66, v184, v66
	v_add_f32_e32 v67, v217, v67
	v_add_f32_e32 v64, v220, v64
	v_add_f32_e32 v65, v221, v65
	v_add_f32_e32 v66, v218, v66
	v_add_f32_e32 v67, v219, v67
	v_add_f32_e32 v64, v65, v64
	v_add_f32_e32 v65, v66, v67
	v_mfma_scale_f32_32x32x64_f8f6f4 v[80:95], v[144:151], v[128:135], v[80:95], v201, v200 op_sel_hi:[0,0,0]
	ds_read_b128 v[136:139], v164 offset:128
	ds_read_b128 v[140:143], v164 offset:144
	ds_read_b128 v[144:147], v164 offset:6784
	ds_read_b128 v[148:151], v164 offset:6800
	v_add_f32_e32 v182, v65, v64
	v_mov_b32_e32 v183, v182
	v_cvt_pk_fp8_f32 v232, v215, v216
	v_cvt_pk_fp8_f32 v236, v228, v230
	v_cvt_pk_fp8_f32 v233, v213, v214
	v_cvt_pk_fp8_f32 v237, v229, v231
	v_cvt_pk_fp8_f32 v234, v194, v211
	v_cvt_pk_fp8_f32 v238, v224, v225
	v_cvt_pk_fp8_f32 v235, v191, v193
	v_cvt_pk_fp8_f32 v239, v220, v221
	v_permlane32_swap_b32_e32 v182, v183
	s_waitcnt lgkmcnt(0)
	v_mfma_scale_f32_32x32x64_f8f6f4 v[96:111], v[136:143], v[112:119], v[96:111], v201, v200 op_sel_hi:[0,0,0]
	v_cvt_pk_fp8_f32 v232, v190, v192 op_sel:[0,0,1]
	v_cvt_pk_fp8_f32 v236, v222, v223 op_sel:[0,0,1]
	v_cvt_pk_fp8_f32 v233, v195, v212 op_sel:[0,0,1]
	v_cvt_pk_fp8_f32 v237, v226, v227 op_sel:[0,0,1]
	v_cvt_pk_fp8_f32 v234, v186, v187 op_sel:[0,0,1]
	v_cvt_pk_fp8_f32 v238, v184, v217 op_sel:[0,0,1]
	v_cvt_pk_fp8_f32 v235, v188, v189 op_sel:[0,0,1]
	v_cvt_pk_fp8_f32 v239, v218, v219 op_sel:[0,0,1]
	v_mfma_scale_f32_32x32x64_f8f6f4 v[80:95], v[144:151], v[112:119], v[80:95], v201, v200 op_sel_hi:[0,0,0]
	s_mul_i32 s15, s10, 0x5c00
	s_add_i32 s11, s15, 0
	v_add_u32_e32 v64, s11, v161
	v_add_u32_e32 v176, v64, v179
	ds_read_b128 v[144:147], v176 offset:13312
	ds_read_b128 v[148:151], v176 offset:13328
	ds_read_b128 v[136:139], v176 offset:15872
	ds_read_b128 v[140:143], v176 offset:15888
	ds_read_b128 v[72:75], v176 offset:18432
	ds_read_b128 v[76:79], v176 offset:18448
	ds_read_b128 v[64:67], v176 offset:20992
	ds_read_b128 v[68:71], v176 offset:21008
	v_max_f32_e32 v164, v96, v97
	v_max3_f32 v165, v99, v100, v101
	v_max3_f32 v164, v164, v98, v108
	v_max3_f32 v165, v165, v110, v111
	v_max3_f32 v166, v102, v103, v104
	v_max3_f32 v167, v105, v106, v107
	s_waitcnt lgkmcnt(0)
	v_mfma_scale_f32_32x32x64_f8f6f4 v[0:15], v[232:239], v[144:151], v[0:15], v201, v201 op_sel_hi:[0,0,0]
	v_max3_f32 v164, v164, v109, v84
	v_max3_f32 v165, v165, v86, v87
	v_max3_f32 v166, v166, v80, v81
	v_max3_f32 v167, v167, v82, v83
	v_max3_f32 v164, v164, v85, v92
	v_max3_f32 v165, v165, v94, v95
	v_max3_f32 v166, v166, v88, v89
	v_max3_f32 v167, v167, v90, v91
	v_mfma_scale_f32_32x32x64_f8f6f4 v[48:63], v[232:239], v[136:143], v[48:63], v201, v201 op_sel_hi:[0,0,0]
	v_max3_f32 v164, v164, v93, v165
	v_max3_f32 v164, v164, v166, v167
	s_mov_b32 s0, 0x410c551d
	v_cmp_ge_f32_e32 vcc, s0, v164
	s_cmp_eq_u64 vcc, exec
	v_mov_b32_e32 v185, 1.0
	s_cbranch_scc0 .LBB0_570

; __device__ __forceinline__ void partialSM(f32x16& p0, f32x16& p1, float& m_reg, float& alpha, const bool first) {
;     float ma = max3f(p0[0], p0[1], p0[2]), mb = max3f(p0[3], p0[4], p0[5]), mc = max3f(p0[6], p0[7], p0[8]), md = max3f(p0[9], p0[10], p0[11]);
;     ma = max3f(ma, p0[12], p0[13]); mb = max3f(mb, p0[14], p0[15]); mc = max3f(mc, p1[0], p1[1]); md = max3f(md, p1[2], p1[3]);
;     ma = max3f(ma, p1[4], p1[5]); mb = max3f(mb, p1[6], p1[7]); mc = max3f(mc, p1[8], p1[9]); md = max3f(md, p1[10], p1[11]);
;     ma = max3f(ma, p1[12], p1[13]); mb = max3f(mb, p1[14], p1[15]);
;     float pmax = fmaxf(max3f(ma, mb, mc), md);
;     { auto rr = __builtin_amdgcn_permlane32_swap(__float_as_uint(pmax), __float_as_uint(pmax), false, false);
;       pmax = fmaxf(__uint_as_float(rr[0]), __uint_as_float(rr[1])); }
;     const float u = pmax - PSH;
;     if (__builtin_expect(!first && __all(u <= THR2), 1)) { alpha = 1.f; }
;     else { const float dl = first ? u : fmaxf(u, 0.f); alpha = __builtin_amdgcn_exp2f(-dl); m_reg += dl;
; #pragma unroll
;         for (int r = 0; r < 16; ++r) { p0[r] -= dl; p1[r] -= dl; } }
; #pragma unroll
;     for (int r = 0; r < 16; ++r) p0[r] = __builtin_amdgcn_exp2f(p0[r]);
; }
; __device__ __forceinline__ void finishSM(f32x16& p0, f32x16& p1, float alpha, float& l_reg, v8i& pa) {
; #pragma unroll
;     for (int r = 0; r < 16; ++r) p1[r] = __builtin_amdgcn_exp2f(p1[r]);
;     float sa = p0[0] + p0[1], sb = p0[2] + p0[3], sc = p0[4] + p0[5], sd = p0[6] + p0[7];
;     sa += p0[8]; sb += p0[9]; sc += p0[10]; sd += p0[11]; sa += p0[12]; sb += p0[13]; sc += p0[14]; sd += p0[15];
; #pragma unroll
;     for (int r = 0; r < 16; r += 4) { sa += p1[r]; sb += p1[r + 1]; sc += p1[r + 2]; sd += p1[r + 3]; }
;     float ps = (sa + sb) + (sc + sd);
;     { auto rr = __builtin_amdgcn_permlane32_swap(__float_as_uint(ps), __float_as_uint(ps), false, false);
;       ps = __uint_as_float(rr[0]) + __uint_as_float(rr[1]); }
;     l_reg = l_reg * alpha + ps;
; #pragma unroll
;     for (int c = 0; c < 4; ++c) { pa[c] = (int)pk4_fp8(p0[4 * c], p0[4 * c + 1], p0[4 * c + 2], p0[4 * c + 3]);
;         pa[4 + c] = (int)pk4_fp8(p1[4 * c], p1[4 * c + 1], p1[4 * c + 2], p1[4 * c + 3]); }
; }
; __device__ __forceinline__ void qkt(f32x16& p0, f32x16& p1, const float m_reg, const char* Ks, const v8i* q8, int r32, int hi) {
;     { const float ini = PSH - m_reg;
.LBB0_563:
	v_sub_f32_e32 v64, 0x40400000, v180
	v_mov_b32_e32 v65, v64
	v_mov_b64_e32 v[66:67], v[64:65]
	v_mov_b64_e32 v[68:69], v[64:65]
	v_mov_b64_e32 v[70:71], v[64:65]
	v_mov_b64_e32 v[72:73], v[64:65]
	v_mov_b64_e32 v[74:75], v[64:65]
	v_mov_b64_e32 v[76:77], v[64:65]
	v_mov_b64_e32 v[78:79], v[64:65]
	v_exp_f32_e32 v231, v80
	v_exp_f32_e32 v233, v81
	s_waitcnt lgkmcnt(0)
	v_mfma_scale_f32_32x32x64_f8f6f4 v[96:111], v[96:103], v[120:127], v[64:79], v201, v200 op_sel_hi:[0,0,0]
	v_exp_f32_e32 v225, v82
	v_exp_f32_e32 v226, v83
	v_exp_f32_e32 v232, v84
	v_exp_f32_e32 v234, v85
	v_exp_f32_e32 v229, v86
	v_exp_f32_e32 v230, v87
	v_add_f32_e32 v80, v216, v215
	v_add_f32_e32 v81, v194, v192
	v_add_f32_e32 v82, v214, v213
	v_add_f32_e32 v83, v212, v211
	v_exp_f32_e32 v227, v88
	v_exp_f32_e32 v228, v89
	v_exp_f32_e32 v219, v90
	v_exp_f32_e32 v220, v91
	v_add_f32_e32 v80, v193, v80
	v_mfma_scale_f32_32x32x64_f8f6f4 v[64:79], v[136:143], v[120:127], v[64:79], v201, v200 op_sel_hi:[0,0,0]
	ds_read_b128 v[136:139], v164 offset:64
	ds_read_b128 v[140:143], v164 offset:80
	ds_read_b128 v[144:147], v164 offset:6720
	ds_read_b128 v[148:151], v164 offset:6736
	v_add_f32_e32 v81, v195, v81
	v_add_f32_e32 v82, v186, v82
	v_add_f32_e32 v83, v187, v83
	v_exp_f32_e32 v223, v92
	v_exp_f32_e32 v224, v93
	v_exp_f32_e32 v221, v94
	v_exp_f32_e32 v222, v95
	v_add_f32_e32 v80, v190, v80
	v_add_f32_e32 v81, v191, v81
	v_add_f32_e32 v82, v188, v82
	v_add_f32_e32 v83, v189, v83
	v_add_f32_e32 v80, v80, v231
	v_add_f32_e32 v81, v81, v233
	v_add_f32_e32 v82, v82, v225
	s_waitcnt lgkmcnt(0)
	v_mfma_scale_f32_32x32x64_f8f6f4 v[96:111], v[136:143], v[128:135], v[96:111], v201, v200 op_sel_hi:[0,0,0]
	v_add_f32_e32 v83, v83, v226
	v_add_f32_e32 v80, v232, v80
	v_add_f32_e32 v81, v234, v81
	v_add_f32_e32 v82, v229, v82
	v_add_f32_e32 v83, v230, v83
	v_add_f32_e32 v80, v227, v80
	v_add_f32_e32 v81, v228, v81
	v_add_f32_e32 v82, v219, v82
	v_add_f32_e32 v83, v220, v83
	v_add_f32_e32 v80, v223, v80
	v_add_f32_e32 v81, v224, v81
	v_add_f32_e32 v82, v221, v82
	v_add_f32_e32 v83, v222, v83
	v_add_f32_e32 v80, v81, v80
	v_add_f32_e32 v81, v82, v83
	v_mfma_scale_f32_32x32x64_f8f6f4 v[64:79], v[144:151], v[128:135], v[64:79], v201, v200 op_sel_hi:[0,0,0]
	ds_read_b128 v[136:139], v164 offset:128
	ds_read_b128 v[140:143], v164 offset:144
	ds_read_b128 v[144:147], v164 offset:6784
	ds_read_b128 v[148:151], v164 offset:6800
	v_add_f32_e32 v217, v81, v80
	v_mov_b32_e32 v218, v217
	v_cvt_pk_fp8_f32 v236, v215, v216
	v_cvt_pk_fp8_f32 v240, v231, v233
	v_cvt_pk_fp8_f32 v237, v213, v214
	v_cvt_pk_fp8_f32 v241, v232, v234
	v_cvt_pk_fp8_f32 v238, v193, v195
	v_cvt_pk_fp8_f32 v242, v227, v228
	v_cvt_pk_fp8_f32 v239, v190, v191
	v_cvt_pk_fp8_f32 v243, v223, v224
	v_permlane32_swap_b32_e32 v217, v218
	s_waitcnt lgkmcnt(0)
	v_mfma_scale_f32_32x32x64_f8f6f4 v[96:111], v[136:143], v[112:119], v[96:111], v201, v200 op_sel_hi:[0,0,0]
	v_cvt_pk_fp8_f32 v236, v192, v194 op_sel:[0,0,1]
	v_cvt_pk_fp8_f32 v240, v225, v226 op_sel:[0,0,1]
	v_cvt_pk_fp8_f32 v237, v211, v212 op_sel:[0,0,1]
	v_cvt_pk_fp8_f32 v241, v229, v230 op_sel:[0,0,1]
	v_cvt_pk_fp8_f32 v238, v186, v187 op_sel:[0,0,1]
	v_cvt_pk_fp8_f32 v242, v219, v220 op_sel:[0,0,1]
	v_cvt_pk_fp8_f32 v239, v188, v189 op_sel:[0,0,1]
	v_cvt_pk_fp8_f32 v243, v221, v222 op_sel:[0,0,1]
	v_mfma_scale_f32_32x32x64_f8f6f4 v[64:79], v[144:151], v[112:119], v[64:79], v201, v200 op_sel_hi:[0,0,0]
	v_add3_u32 v84, s12, v161, v179
	ds_read_b128 v[144:147], v84 offset:13312
	ds_read_b128 v[148:151], v84 offset:13328
	ds_read_b128 v[136:139], v84 offset:15872
	ds_read_b128 v[140:143], v84 offset:15888
	ds_read_b128 v[88:91], v84 offset:18432
	ds_read_b128 v[92:95], v84 offset:18448
	ds_read_b128 v[80:83], v84 offset:20992
	ds_read_b128 v[84:87], v84 offset:21008
	s_nop 2
	v_max_f32_e32 v164, v96, v97
	v_max3_f32 v165, v99, v100, v101
	v_max3_f32 v164, v164, v98, v108
	v_max3_f32 v165, v165, v110, v111
	v_max3_f32 v166, v102, v103, v104
	v_max3_f32 v167, v105, v106, v107
	s_waitcnt lgkmcnt(0)
	v_mfma_scale_f32_32x32x64_f8f6f4 v[0:15], v[236:243], v[144:151], v[0:15], v201, v201 op_sel_hi:[0,0,0]
	v_max3_f32 v164, v164, v109, v68
	v_max3_f32 v165, v165, v70, v71
	v_max3_f32 v166, v166, v64, v65
	v_max3_f32 v167, v167, v66, v67
	v_max3_f32 v164, v164, v69, v76
	v_max3_f32 v165, v165, v78, v79
	v_max3_f32 v166, v166, v72, v73
	v_max3_f32 v167, v167, v74, v75
	v_mfma_scale_f32_32x32x64_f8f6f4 v[48:63], v[236:243], v[136:143], v[48:63], v201, v201 op_sel_hi:[0,0,0]
	v_max3_f32 v164, v164, v77, v165
	v_max3_f32 v164, v164, v166, v167
	s_mov_b32 s0, 0x410c551d
	v_cmp_ge_f32_e32 vcc, s0, v164
	s_cmp_eq_u64 vcc, exec
	v_mov_b32_e32 v184, 1.0
	s_cbranch_scc0 .LBB0_571

; #define PG8_STAGE_B(bufoff, gbase) do { _Pragma("unroll") for (int _i = 0; _i < 2; ++_i) \
;         __builtin_amdgcn_global_load_lds((const unsigned*)((const char*)(gbase) + voffB[_i]), (LAS unsigned*)(lds + (bufoff) + ldsw + _i * 8192), 16, 0, 0); } while (0)
; #define PG8_STAGE_A(bufoff, gbase, UA) do { _Pragma("unroll") for (int _i = 0; _i < 2; ++_i) \
;         __builtin_amdgcn_global_load_lds((const unsigned*)((const char*)(gbase) + (UA)[_i]), (LAS unsigned*)(lds + (bufoff) + ldsw + _i * 8192), 16, 0, 0); } while (0)
; #define PG8_WAIT_V(n) asm volatile("s_waitcnt vmcnt(" #n ")" ::: "memory")
; #define PG8_BAR __builtin_amdgcn_s_barrier()
; template <class Epi, class Sched, bool GATHER, bool FP8 = false>
; __device__ __forceinline__ void gemm_phase(LAS unsigned char* lds, const Gemm g, const Sched& S, const Epi& E, const int wave_s) {
;     ...
;     f32x4 acc[2][2][4][2];
; #pragma unroll
;     for (int a = 0; a < 2; ++a)
; #pragma unroll
;         for (int b = 0; b < 2; ++b)
; #pragma unroll
;             for (int m = 0; m < 4; ++m)
; #pragma unroll
;                 for (int n = 0; n < 2; ++n) acc[a][b][m][n] = (f32x4){0.f, 0.f, 0.f, 0.f};
;     v8i At[4], B0[2], B1[2];
;     const char* cA = GATHER ? (const char*)g.A : (const char*)g.A + (size_t)cur.pm * tstepA;
;     const char* cB = (const char*)g.Bt + (size_t)cur.pn * tstepB;
;     PG8_STAGE_B(PG8_SB(0, 0), cB); PG8_STAGE_B(PG8_SB(0, 1), cB + hstepB); PG8_STAGE_A(PG8_SA(0, 0), cA, uAc[0]); PG8_STAGE_A(PG8_SA(0, 1), cA, uAc[1]);
;     if (wr == 1) PG8_BAR;
;     PG8_WAIT_V(2); PG8_BAR;
;     PG8_STAGE_B(PG8_SB(1, 0), cB + kstep); PG8_STAGE_A(PG8_SA(1, 0), cA + kstep, uAc[0]); PG8_STAGE_B(PG8_SB(1, 1), cB + hstepB + kstep);
;     PG8_WAIT_V(6); PG8_BAR;
.LBB0_653:
	v_lshrrev_b32_e32 v16, 1, v7
	v_and_b32_e32 v145, 24, v16
	s_lshl_b32 s1, s8, 5
	v_and_b32_e32 v11, 15, v7
	v_lshlrev_b32_e32 v16, 1, v145
	v_lshlrev_b32_e32 v7, 2, v7
	s_and_b32 s17, s1, 0x60
	v_lshl_or_b32 v144, s0, 6, v11
	v_lshl_or_b32 v11, v11, 6, v16
	v_and_b32_e32 v7, 32, v7
	s_lshl_b32 s0, s0, 13
	s_lshl_b32 s1, s17, 7
	v_readlane_b32 s20, v248, 55
	v_bitop3_b32 v16, v11, s0, v7 bitop3:0xde
	s_add_u32 s0, s6, 0x40080
	v_mov_b32_e32 v133, v153
	v_readlane_b32 s21, v248, 56
	v_bitop3_b32 v146, v11, s1, v7 bitop3:0xde
	s_addc_u32 s1, s7, 0
	s_add_i32 m0, s13, 0x18000
	v_lshl_add_u64 v[0:1], v[0:1], 0, s[96:97]
	v_lshl_add_u64 v[12:13], s[20:21], 0, v[132:133]
	v_mov_b32_e32 v135, v153
	s_waitcnt vmcnt(2)
	s_barrier
	global_load_lds_dwordx4 v[0:1], off
	v_lshl_add_u64 v[0:1], v[2:3], 0, s[96:97]
	s_add_i32 m0, s13, 0x1a000
	s_add_i32 s18, s13, 0x8000
	v_lshl_add_u64 v[14:15], s[20:21], 0, v[134:135]
	global_load_lds_dwordx4 v[0:1], off
	v_lshl_add_u64 v[0:1], v[12:13], 0, s[96:97]
	s_mov_b32 m0, s18
	s_add_i32 s19, s13, 0xa000
	global_load_lds_dwordx4 v[0:1], off
	v_lshl_add_u64 v[0:1], v[14:15], 0, s[96:97]
	s_mov_b32 m0, s19
	s_mov_b32 s2, 0x40000
	global_load_lds_dwordx4 v[0:1], off
	s_add_i32 m0, s13, 0x1c000
	v_lshl_add_u64 v[0:1], s[0:1], 0, v[152:153]
	global_load_lds_dwordx4 v[0:1], off
	v_lshl_add_u64 v[0:1], s[0:1], 0, v[130:131]
	s_add_i32 m0, s13, 0x1e000
	v_readlane_b32 s0, v252, 5
	global_load_lds_dwordx4 v[0:1], off
	v_lshlrev_b32_e32 v0, 14, v8
	v_and_b32_e32 v0, 0xffff8000, v0
	v_lshl_add_u32 v0, v9, 11, v0
	v_and_b32_e32 v1, 1, v8
	v_lshl_or_b32 v0, v1, 6, v0
	v_lshlrev_b32_e32 v1, 1, v10
	v_add3_u32 v0, v0, v1, s2
	v_mov_b32_e32 v1, v153
	v_readlane_b32 s1, v252, 6
	s_waitcnt vmcnt(6)
	v_mov_b32_e32 v8, 0
	v_mov_b32_e32 v137, v153
	v_lshl_add_u64 v[140:141], s[0:1], 0, v[0:1]
	v_lshlrev_b32_e32 v0, 14, v4
	v_and_b32_e32 v0, 0xffff8000, v0
	v_lshl_add_u32 v0, v5, 11, v0
	v_and_b32_e32 v1, 1, v4
	v_lshl_or_b32 v0, v1, 6, v0
	v_lshlrev_b32_e32 v1, 1, v6
	v_add3_u32 v0, v0, v1, s2
	v_mov_b32_e32 v1, v153
	v_mov_b32_e32 v139, v153
	v_lshl_add_u64 v[142:143], s[0:1], 0, v[0:1]
	s_mov_b32 s31, -2
	s_mov_b64 s[8:9], 0
	v_add_u32_e32 v147, 0, v16
	v_mov_b32_e32 v9, v8
	v_mov_b64_e32 v[10:11], 0
	v_mov_b64_e32 v[16:17], 0
	v_mov_b64_e32 v[18:19], 0
	v_mov_b64_e32 v[32:33], 0
	v_mov_b64_e32 v[34:35], 0
	v_mov_b64_e32 v[40:41], 0
	v_mov_b64_e32 v[42:43], 0
	v_mov_b64_e32 v[0:1], 0
	v_mov_b64_e32 v[2:3], 0
	v_mov_b64_e32 v[4:5], 0
	v_mov_b64_e32 v[6:7], 0
	v_mov_b64_e32 v[12:13], 0
	v_mov_b64_e32 v[14:15], 0
	v_mov_b64_e32 v[20:21], 0
	v_mov_b64_e32 v[22:23], 0
	v_mov_b64_e32 v[36:37], 0
	v_mov_b64_e32 v[38:39], 0
	v_mov_b64_e32 v[44:45], 0
	v_mov_b64_e32 v[46:47], 0
	v_mov_b64_e32 v[56:57], 0
	v_mov_b64_e32 v[58:59], 0
	v_mov_b64_e32 v[60:61], 0
	v_mov_b64_e32 v[62:63], 0
	v_mov_b64_e32 v[64:65], 0
	v_mov_b64_e32 v[66:67], 0
	v_mov_b64_e32 v[68:69], 0
	v_mov_b64_e32 v[70:71], 0
	v_mov_b64_e32 v[76:77], 0
	v_mov_b64_e32 v[78:79], 0
	v_mov_b64_e32 v[84:85], 0
	v_mov_b64_e32 v[86:87], 0
	v_mov_b64_e32 v[88:89], 0
	v_mov_b64_e32 v[90:91], 0
	v_mov_b64_e32 v[96:97], 0
	v_mov_b64_e32 v[98:99], 0
	v_mov_b64_e32 v[104:105], 0
	v_mov_b64_e32 v[106:107], 0
	v_mov_b64_e32 v[112:113], 0
	v_mov_b64_e32 v[114:115], 0
	v_mov_b64_e32 v[72:73], 0
	v_mov_b64_e32 v[74:75], 0
	v_mov_b64_e32 v[80:81], 0
	v_mov_b64_e32 v[82:83], 0
	v_mov_b64_e32 v[92:93], 0
	v_mov_b64_e32 v[94:95], 0
	v_mov_b64_e32 v[100:101], 0
	v_mov_b64_e32 v[102:103], 0
	v_mov_b64_e32 v[108:109], 0
	v_mov_b64_e32 v[110:111], 0
	v_mov_b64_e32 v[116:117], 0
	v_mov_b64_e32 v[118:119], 0
	v_mov_b64_e32 v[120:121], 0
	v_mov_b64_e32 v[122:123], 0
	v_mov_b64_e32 v[124:125], 0
	v_mov_b64_e32 v[126:127], 0
	v_mov_b64_e32 v[52:53], 0
	v_mov_b64_e32 v[54:55], 0
	v_mov_b64_e32 v[48:49], 0
	v_mov_b64_e32 v[50:51], 0
	v_mov_b64_e32 v[28:29], 0
	v_mov_b64_e32 v[30:31], 0
	v_mov_b64_e32 v[24:25], 0
	v_mov_b64_e32 v[26:27], 0
	v_readlane_b32 s41, v252, 4
	v_readlane_b32 s42, v252, 7
	v_readlane_b32 s43, v252, 8
	s_barrier

; template <class Epi, class Sched, bool GATHER, bool FP8 = false>
; __device__ __forceinline__ void gemm_phase(LAS unsigned char* lds, const Gemm g, const Sched& S, const Epi& E, const int wave_s) {
;     ...
;         const bool has_next = S.next(ui + 1, nxt);
;         const char* nB = has_next ? (const char*)g.Bt + (size_t)nxt.pn * tstepB : cB;
;         const char* nA = (GATHER || !has_next) ? cA : (const char*)g.A + (size_t)nxt.pm * tstepA;
;     ...
; #pragma unroll
;         for (int a = 0; a < 2; ++a)
; #pragma unroll
;             for (int b = 0; b < 2; ++b)
; #pragma unroll
;                 for (int m = 0; m < 4; ++m)
; #pragma unroll
;                     for (int n = 0; n < 2; ++n) acc[a][b][m][n] = (f32x4){0.f, 0.f, 0.f, 0.f};
;         cur = nxt; cB = nB; cA = nA; ++ui;
.LBB0_764:
	s_ashr_i32 s13, s12, 31
	s_lshl_b64 s[2:3], s[12:13], 19
	s_add_u32 s16, s31, s2
	s_addc_u32 s17, s46, s3
	s_and_b64 s[2:3], s[40:41], exec
	s_cselect_b32 s13, s17, s45
	s_cselect_b32 s56, s16, s44
	s_ashr_i32 s15, s14, 31
	s_lshl_b64 s[2:3], s[14:15], 19
	v_readlane_b32 s4, v249, 26
	s_add_u32 s18, s4, s2
	v_readlane_b32 s2, v249, 27
	s_addc_u32 s19, s2, s3
	s_and_b64 s[2:3], s[40:41], exec
	s_cselect_b32 s15, s19, s1
	s_cselect_b32 s57, s18, s0
	s_add_u32 s42, s0, 0x80
	s_addc_u32 s43, s1, 0
	s_add_u32 s58, s44, 0x100
	v_mov_b32_e32 v8, 0
	s_addc_u32 s59, s45, 0
	s_mov_b32 s60, -2
	v_mov_b32_e32 v9, v8
	v_mov_b64_e32 v[10:11], 0
	v_mov_b64_e32 v[16:17], 0
	v_mov_b64_e32 v[18:19], 0
	v_mov_b64_e32 v[32:33], 0
	v_mov_b64_e32 v[34:35], 0
	v_mov_b64_e32 v[40:41], 0
	v_mov_b64_e32 v[42:43], 0
	v_mov_b64_e32 v[0:1], 0
	v_mov_b64_e32 v[2:3], 0
	v_mov_b64_e32 v[4:5], 0
	v_mov_b64_e32 v[6:7], 0
	v_mov_b64_e32 v[12:13], 0
	v_mov_b64_e32 v[14:15], 0
	v_mov_b64_e32 v[20:21], 0
	v_mov_b64_e32 v[22:23], 0
	v_mov_b64_e32 v[36:37], 0
	v_mov_b64_e32 v[38:39], 0
	v_mov_b64_e32 v[44:45], 0
	v_mov_b64_e32 v[46:47], 0
	v_mov_b64_e32 v[56:57], 0
	v_mov_b64_e32 v[58:59], 0
	v_mov_b64_e32 v[60:61], 0
	v_mov_b64_e32 v[62:63], 0
	v_mov_b64_e32 v[64:65], 0
	v_mov_b64_e32 v[66:67], 0
	v_mov_b64_e32 v[68:69], 0
	v_mov_b64_e32 v[70:71], 0
	v_mov_b64_e32 v[76:77], 0
	v_mov_b64_e32 v[78:79], 0
	v_mov_b64_e32 v[84:85], 0
	v_mov_b64_e32 v[86:87], 0
	v_mov_b64_e32 v[88:89], 0
	v_mov_b64_e32 v[90:91], 0
	v_mov_b64_e32 v[96:97], 0
	v_mov_b64_e32 v[98:99], 0
	v_mov_b64_e32 v[104:105], 0
	v_mov_b64_e32 v[106:107], 0
	v_mov_b64_e32 v[112:113], 0
	v_mov_b64_e32 v[114:115], 0
	v_mov_b64_e32 v[72:73], 0
	v_mov_b64_e32 v[74:75], 0
	v_mov_b64_e32 v[80:81], 0
	v_mov_b64_e32 v[82:83], 0
	v_mov_b64_e32 v[92:93], 0
	v_mov_b64_e32 v[94:95], 0
	v_mov_b64_e32 v[100:101], 0
	v_mov_b64_e32 v[102:103], 0
	v_mov_b64_e32 v[108:109], 0
	v_mov_b64_e32 v[110:111], 0
	v_mov_b64_e32 v[116:117], 0
	v_mov_b64_e32 v[118:119], 0
	v_mov_b64_e32 v[120:121], 0
	v_mov_b64_e32 v[122:123], 0
	v_mov_b64_e32 v[124:125], 0
	v_mov_b64_e32 v[126:127], 0
	v_mov_b64_e32 v[52:53], 0
	v_mov_b64_e32 v[54:55], 0
	v_mov_b64_e32 v[48:49], 0
	v_mov_b64_e32 v[50:51], 0
	v_mov_b64_e32 v[28:29], 0
	v_mov_b64_e32 v[30:31], 0
	v_mov_b64_e32 v[24:25], 0
	v_mov_b64_e32 v[26:27], 0

; template <class Epi, class Sched, bool GATHER, bool FP8 = false>
; __device__ __forceinline__ void gemm_phase(LAS unsigned char* lds, const Gemm g, const Sched& S, const Epi& E, const int wave_s) {
;     ...
;         const bool has_next = S.next(ui + 1, nxt);
;         const char* nB = has_next ? (const char*)g.Bt + (size_t)nxt.pn * tstepB : cB;
;         const char* nA = (GATHER || !has_next) ? cA : (const char*)g.A + (size_t)nxt.pm * tstepA;
;     ...
; #pragma unroll
;         for (int a = 0; a < 2; ++a)
; #pragma unroll
;             for (int b = 0; b < 2; ++b)
; #pragma unroll
;                 for (int m = 0; m < 4; ++m)
; #pragma unroll
;                     for (int n = 0; n < 2; ++n) acc[a][b][m][n] = (f32x4){0.f, 0.f, 0.f, 0.f};
;         cur = nxt; cB = nB; cA = nA; ++ui;
.LBB0_1470:
	s_ashr_i32 s17, s16, 31
	s_lshl_b64 s[0:1], s[16:17], 18
	s_add_u32 s18, s55, s0
	s_addc_u32 s19, s56, s1
	s_and_b64 s[0:1], s[42:43], exec
	v_readlane_b32 s2, v249, 16
	s_cselect_b32 s0, s19, s47
	s_cselect_b32 s1, s18, s46
	v_mov_b32_e32 v181, v153
	v_mov_b32_e32 v183, v153
	v_readlane_b32 s3, v249, 17
	s_add_u32 s17, s46, 0x100
	v_mov_b32_e32 v36, 0
	v_lshl_add_u64 v[184:185], s[2:3], 0, v[182:183]
	v_lshl_add_u64 v[186:187], s[2:3], 0, v[180:181]
	s_addc_u32 s66, s47, 0
	s_mov_b32 s67, -2
	s_mov_b64 s[42:43], 0
	v_mov_b32_e32 v37, v36
	v_mov_b64_e32 v[38:39], 0
	v_mov_b64_e32 v[32:33], 0
	v_mov_b64_e32 v[34:35], 0
	v_mov_b64_e32 v[48:49], 0
	v_mov_b64_e32 v[50:51], 0
	v_mov_b64_e32 v[52:53], 0
	v_mov_b64_e32 v[54:55], 0
	v_mov_b64_e32 v[64:65], 0
	v_mov_b64_e32 v[66:67], 0
	v_mov_b64_e32 v[68:69], 0
	v_mov_b64_e32 v[70:71], 0
	v_mov_b64_e32 v[80:81], 0
	v_mov_b64_e32 v[82:83], 0
	v_mov_b64_e32 v[84:85], 0
	v_mov_b64_e32 v[86:87], 0
	v_mov_b64_e32 v[40:41], 0
	v_mov_b64_e32 v[42:43], 0
	v_mov_b64_e32 v[44:45], 0
	v_mov_b64_e32 v[46:47], 0
	v_mov_b64_e32 v[56:57], 0
	v_mov_b64_e32 v[58:59], 0
	v_mov_b64_e32 v[60:61], 0
	v_mov_b64_e32 v[62:63], 0
	v_mov_b64_e32 v[72:73], 0
	v_mov_b64_e32 v[74:75], 0
	v_mov_b64_e32 v[76:77], 0
	v_mov_b64_e32 v[78:79], 0
	v_mov_b64_e32 v[88:89], 0
	v_mov_b64_e32 v[90:91], 0
	v_mov_b64_e32 v[92:93], 0
	v_mov_b64_e32 v[94:95], 0
	v_mov_b64_e32 v[96:97], 0
	v_mov_b64_e32 v[98:99], 0
	v_mov_b64_e32 v[100:101], 0
	v_mov_b64_e32 v[102:103], 0
	v_mov_b64_e32 v[112:113], 0
	v_mov_b64_e32 v[114:115], 0
	v_mov_b64_e32 v[116:117], 0
	v_mov_b64_e32 v[118:119], 0
	v_mov_b64_e32 v[128:129], 0
	v_mov_b64_e32 v[130:131], 0
	v_mov_b64_e32 v[132:133], 0
	v_mov_b64_e32 v[134:135], 0
	v_mov_b64_e32 v[144:145], 0
	v_mov_b64_e32 v[146:147], 0
	v_mov_b64_e32 v[148:149], 0
	v_mov_b64_e32 v[150:151], 0
	v_mov_b64_e32 v[104:105], 0
	v_mov_b64_e32 v[106:107], 0
	v_mov_b64_e32 v[108:109], 0
	v_mov_b64_e32 v[110:111], 0
	v_mov_b64_e32 v[120:121], 0
	v_mov_b64_e32 v[122:123], 0
	v_mov_b64_e32 v[124:125], 0
	v_mov_b64_e32 v[126:127], 0
	v_mov_b64_e32 v[136:137], 0
	v_mov_b64_e32 v[138:139], 0
	v_mov_b64_e32 v[140:141], 0
	v_mov_b64_e32 v[142:143], 0
	v_mov_b64_e32 v[154:155], 0
	v_mov_b64_e32 v[156:157], 0
	v_mov_b64_e32 v[158:159], 0
	v_mov_b64_e32 v[160:161], 0

; template <class Epi, class Sched, bool GATHER, bool FP8 = false>
; __device__ __forceinline__ void gemm_phase(LAS unsigned char* lds, const Gemm g, const Sched& S, const Epi& E, const int wave_s) {
;     ...
;         const bool has_next = S.next(ui + 1, nxt);
;         const char* nB = has_next ? (const char*)g.Bt + (size_t)nxt.pn * tstepB : cB;
;         const char* nA = (GATHER || !has_next) ? cA : (const char*)g.A + (size_t)nxt.pm * tstepA;
;     ...
; #pragma unroll
;         for (int a = 0; a < 2; ++a)
; #pragma unroll
;             for (int b = 0; b < 2; ++b)
; #pragma unroll
;                 for (int m = 0; m < 4; ++m)
; #pragma unroll
;                     for (int n = 0; n < 2; ++n) acc[a][b][m][n] = (f32x4){0.f, 0.f, 0.f, 0.f};
;         cur = nxt; cB = nB; cA = nA; ++ui;
.LBB0_1570:
	s_ashr_i32 s19, s18, 31
	s_lshl_b64 s[0:1], s[18:19], 18
	s_add_u32 s42, s64, s0
	s_addc_u32 s43, s65, s1
	s_and_b64 s[0:1], s[40:41], exec
	s_cselect_b32 s0, s43, s53
	s_cselect_b32 s1, s42, s52
	s_ashr_i32 s17, s16, 31
	s_lshl_b64 s[2:3], s[16:17], 18
	v_readlane_b32 s20, v246, 45
	v_readlane_b32 s21, v246, 46
	s_add_u32 s44, s20, s2
	s_addc_u32 s45, s21, s3
	s_and_b64 s[2:3], s[40:41], exec
	s_cselect_b32 s17, s45, s51
	s_cselect_b32 s19, s44, s50
	s_add_u32 s50, s50, 0x80
	s_addc_u32 s51, s51, 0
	s_add_u32 s72, s52, 0x100
	v_mov_b32_e32 v60, 0
	s_addc_u32 s73, s53, 0
	s_mov_b32 s74, -2
	v_mov_b32_e32 v61, v60
	v_mov_b64_e32 v[62:63], 0
	v_mov_b64_e32 v[68:69], 0
	v_mov_b64_e32 v[70:71], 0
	v_mov_b64_e32 v[80:81], 0
	v_mov_b64_e32 v[82:83], 0
	v_mov_b64_e32 v[84:85], 0
	v_mov_b64_e32 v[86:87], 0
	v_mov_b64_e32 v[32:33], 0
	v_mov_b64_e32 v[34:35], 0
	v_mov_b64_e32 v[36:37], 0
	v_mov_b64_e32 v[38:39], 0
	v_mov_b64_e32 v[48:49], 0
	v_mov_b64_e32 v[50:51], 0
	v_mov_b64_e32 v[52:53], 0
	v_mov_b64_e32 v[54:55], 0
	v_mov_b64_e32 v[72:73], 0
	v_mov_b64_e32 v[74:75], 0
	v_mov_b64_e32 v[76:77], 0
	v_mov_b64_e32 v[78:79], 0
	v_mov_b64_e32 v[88:89], 0
	v_mov_b64_e32 v[90:91], 0
	v_mov_b64_e32 v[92:93], 0
	v_mov_b64_e32 v[94:95], 0
	v_mov_b64_e32 v[96:97], 0
	v_mov_b64_e32 v[98:99], 0
	v_mov_b64_e32 v[100:101], 0
	v_mov_b64_e32 v[102:103], 0
	v_mov_b64_e32 v[112:113], 0
	v_mov_b64_e32 v[114:115], 0
	v_mov_b64_e32 v[116:117], 0
	v_mov_b64_e32 v[118:119], 0
	v_mov_b64_e32 v[128:129], 0
	v_mov_b64_e32 v[130:131], 0
	v_mov_b64_e32 v[132:133], 0
	v_mov_b64_e32 v[134:135], 0
	v_mov_b64_e32 v[144:145], 0
	v_mov_b64_e32 v[146:147], 0
	v_mov_b64_e32 v[148:149], 0
	v_mov_b64_e32 v[150:151], 0
	v_mov_b64_e32 v[104:105], 0
	v_mov_b64_e32 v[106:107], 0
	v_mov_b64_e32 v[108:109], 0
	v_mov_b64_e32 v[110:111], 0
	v_mov_b64_e32 v[120:121], 0
	v_mov_b64_e32 v[122:123], 0
	v_mov_b64_e32 v[124:125], 0
	v_mov_b64_e32 v[126:127], 0
	v_mov_b64_e32 v[136:137], 0
	v_mov_b64_e32 v[138:139], 0
	v_mov_b64_e32 v[140:141], 0
	v_mov_b64_e32 v[142:143], 0
	v_mov_b64_e32 v[154:155], 0
	v_mov_b64_e32 v[156:157], 0
	v_mov_b64_e32 v[158:159], 0
	v_mov_b64_e32 v[160:161], 0
	v_mov_b64_e32 v[64:65], 0
	v_mov_b64_e32 v[66:67], 0
	v_mov_b64_e32 v[56:57], 0
	v_mov_b64_e32 v[58:59], 0
	v_mov_b64_e32 v[44:45], 0
	v_mov_b64_e32 v[46:47], 0
	v_mov_b64_e32 v[40:41], 0
	v_mov_b64_e32 v[42:43], 0
